# stick-breaking units stop prefetching K/V tiles once some wave has finished (tiles past the early exit were fetched and drained for nothing); a prefetch is still forced when the next tile is not in fl
# baseline (speedup 1.0000x reference)
; #define AT_WAIT_BAR(NI, n) do { if ((n) >= 2) asm volatile("s_waitcnt vmcnt(%0) lgkmcnt(0)\n\ts_barrier" :: "n"(2 * (NI)) : "memory"); \
;         else if ((n) == 1) asm volatile("s_waitcnt vmcnt(%0) lgkmcnt(0)\n\ts_barrier" :: "n"(NI) : "memory"); \
;         else asm volatile("s_waitcnt vmcnt(0) lgkmcnt(0)\n\ts_barrier" ::: "memory"); } while (0)
; #define SB_ISSUE(i) do { const int j_ = jhi - (i); dma_kv(lds, (i) & 3, Kb + (size_t)j_ * 4096, Vb + (size_t)j_ * 4096, 64, wid, lane); } while (0)
;     ...
;             for (int i = 0; i < T; ++i) {
;                 if (i > 0) {
;                     const int n = issued - 1 - i; AT_WAIT_BAR(2, n);
;                     int c = 0;
; #pragma unroll
;                     for (int k = 0; k < 8; ++k) c += flags[((i - 1) & 1) * 8 + k];
;                     alldone = (c == 8);
;                 }
;                 if (alldone) break;
;                 if (issued < T) { SB_ISSUE(issued); ++issued; }
.LBB0_470:
	s_and_b32 s79, s54, 8
	s_xor_b32 s4, s79, 8
	s_add_i32 s5, 0, 0x21400
	s_lshl_b32 s4, s4, 2
	s_add_i32 s4, s5, s4
	v_mov_b32_e32 v34, s4
	s_xor_b32 s4, s79, 9
	s_lshl_b32 s4, s4, 2
	s_add_i32 s4, s5, s4
	v_mov_b32_e32 v52, s4
	s_xor_b32 s4, s79, 10
	s_lshl_b32 s4, s4, 2
	s_add_i32 s4, s5, s4
	v_mov_b32_e32 v53, s4
	s_xor_b32 s4, s79, 11
	s_lshl_b32 s4, s4, 2
	s_add_i32 s4, s5, s4
	v_mov_b32_e32 v54, s4
	s_xor_b32 s4, s79, 12
	s_lshl_b32 s4, s4, 2
	s_add_i32 s4, s5, s4
	v_mov_b32_e32 v55, s4
	s_xor_b32 s4, s79, 13
	s_lshl_b32 s4, s4, 2
	s_add_i32 s4, s5, s4
	v_mov_b32_e32 v56, s4
	s_xor_b32 s4, s79, 14
	s_lshl_b32 s4, s4, 2
	s_add_i32 s4, s5, s4
	v_mov_b32_e32 v57, s4
	s_xor_b32 s4, s79, 15
	s_lshl_b32 s4, s4, 2
	s_add_i32 s4, s5, s4
	v_mov_b32_e32 v58, s4
	ds_read_b32 v34, v34
	ds_read_b32 v52, v52
	ds_read_b32 v53, v53
	ds_read_b32 v54, v54
	ds_read_b32 v55, v55
	ds_read_b32 v56, v56
	ds_read_b32 v57, v57
	ds_read_b32 v58, v58
	s_waitcnt lgkmcnt(6)
	v_add_u32_e32 v34, v52, v34
	s_waitcnt lgkmcnt(5)
	v_add_u32_e32 v34, v34, v53
	s_waitcnt lgkmcnt(4)
	v_add_u32_e32 v34, v34, v54
	s_waitcnt lgkmcnt(3)
	v_add_u32_e32 v34, v34, v55
	s_waitcnt lgkmcnt(2)
	v_add_u32_e32 v34, v34, v56
	s_waitcnt lgkmcnt(1)
	v_add_u32_e32 v34, v34, v57
	s_waitcnt lgkmcnt(0)
	v_add_u32_e32 v34, v34, v58
	v_cmp_eq_u32_e32 vcc, 8, v34
	s_mov_b64 s[34:35], -1
	s_cbranch_vccnz .LBB0_461
	v_readfirstlane_b32 s4, v34
	s_cmp_eq_u32 s4, 0
	s_cbranch_scc1 .Lsb_issue_chk
	s_cmp_lt_i32 s62, 0
	s_cbranch_scc0 .LBB0_473
.Lsb_issue_chk:
	s_cmp_lt_i32 s36, s39
	s_cbranch_scc1 .LBB0_473
	s_sub_i32 s66, s36, s39
	s_lshl_b32 s4, s39, 13
	s_lshl_b64 s[34:35], s[66:67], 13
	s_and_b32 s4, s4, 0x6000
	v_lshl_add_u64 v[52:53], v[86:87], 0, s[34:35]
	s_add_i32 s5, s4, s24
	s_mov_b32 s14, m0
	s_mov_b32 m0, s5
	s_nop 0
	global_load_lds_dwordx4 v[52:53], off
	s_mov_b32 m0, s14
	v_lshl_add_u64 v[54:55], v[88:89], 0, s[34:35]
	s_add_i32 s4, s4, s44
	s_mov_b32 s5, m0
	s_mov_b32 m0, s4
	s_nop 0
	global_load_lds_dwordx4 v[54:55], off
	s_mov_b32 m0, s5
	s_add_i32 s39, s39, 1
